# speedup vs baseline: 1.0491x; 1.0159x over previous
_Z7fc_gemmPKcS0_PKfS2_Pf:
	s_cmpk_lt_u32 s2, 0x100
	s_cbranch_scc1 .Lfc_exit
	s_sub_u32 s2, s2, 0x100
	s_load_dwordx8 s[4:11], s[0:1], 0x0
	s_load_dwordx2 s[12:13], s[0:1], 0x20
	v_lshrrev_b32_e32 v1, 6, v0
	s_and_b32 s15, s2, 7
	s_lshr_b32 s16, s2, 3
	v_readfirstlane_b32 s14, v1
	v_and_b32_e32 v1, 63, v0
	v_and_b32_e32 v2, 31, v0
	v_bfe_u32 v3, v0, 5, 1
	v_lshrrev_b32_e32 v7, 1, v2
	v_and_b32_e32 v56, 1, v2
	v_lshlrev_b32_e32 v56, 3, v56
	v_xor_b32_e32 v56, v56, v3
	v_xor_b32_e32 v56, v56, v7
	v_lshlrev_b32_e32 v56, 4, v56
	v_lshl_or_b32 v56, v7, 8, v56
	s_lshr_b32 s17, s14, 1
	s_and_b32 s18, s14, 1
	s_lshl_b32 s19, s17, 13
	s_lshl_b32 s27, s18, 13
	s_add_u32 s27, s27, 0x8000
	v_add_u32_e32 v8, s19, v56
	v_add_u32_e32 v12, s27, v56
	v_xor_b32_e32 v9, 32, v8
	v_xor_b32_e32 v13, 32, v12
	v_xor_b32_e32 v10, 64, v8
	v_xor_b32_e32 v14, 64, v12
	v_xor_b32_e32 v11, 96, v8
	v_xor_b32_e32 v15, 96, v12
	v_add_u32_e32 v16, 0x10000, v8
	v_add_u32_e32 v17, 0x10000, v9
	v_add_u32_e32 v18, 0x10000, v10
	v_add_u32_e32 v19, 0x10000, v11
	v_add_u32_e32 v20, 0x10000, v12
	v_add_u32_e32 v21, 0x10000, v13
	v_add_u32_e32 v22, 0x10000, v14
	v_add_u32_e32 v23, 0x10000, v15
	v_lshrrev_b32_e32 v4, 6, v0
	v_lshlrev_b32_e32 v4, 11, v4
	v_lshl_or_b32 v4, v1, 4, v4
	s_lshl_b32 s26, s14, 11
	v_lshlrev_b32_e32 v5, 16, v3
	v_lshl_or_b32 v5, v2, 2, v5
	v_lshlrev_b32_e32 v6, 2, v2
	s_waitcnt lgkmcnt(0)
	s_lshl_b32 s3, s15, 18
	s_add_u32 s20, s4, s3
	s_addc_u32 s21, s5, 0
	s_add_u32 s22, s20, 0x20000
	s_addc_u32 s23, s21, 0
	s_lshl_b32 s3, s16, 17
	s_add_u32 s24, s6, s3
	s_addc_u32 s25, s7, 0
	s_lshl_b32 s3, s16, 9
	s_lshl_b32 s38, s18, 8
	s_add_u32 s3, s3, s38
	s_add_u32 s36, s8, s3
	s_addc_u32 s37, s9, 0
	s_lshl_b32 s38, s15, 22
	s_lshl_b32 s39, s17, 20
	s_add_u32 s38, s38, s39
	s_add_u32 s38, s38, s3
	s_add_u32 s28, s10, s38
	s_addc_u32 s29, s11, 0
	s_add_u32 s30, s12, s38
	s_addc_u32 s31, s13, 0
	global_load_dword v62, v6, s[36:37]
	global_load_dword v63, v6, s[36:37] offset:128
	s_add_u32 m0, s26, 0
	s_nop 0
	global_load_lds_dwordx4 v4, s[20:21]
	global_load_lds_dwordx4 v4, s[20:21] offset:1024
	s_add_u32 m0, s26, 16384
	s_nop 0
	global_load_lds_dwordx4 v4, s[22:23]
	global_load_lds_dwordx4 v4, s[22:23] offset:1024
	s_add_u32 m0, s26, 32768
	s_nop 0
	global_load_lds_dwordx4 v4, s[24:25]
	global_load_lds_dwordx4 v4, s[24:25] offset:1024
	v_add_u32_e32 v4, 0x4000, v4
	s_add_u32 m0, s26, 49152
	s_nop 0
	global_load_lds_dwordx4 v4, s[20:21]
	global_load_lds_dwordx4 v4, s[20:21] offset:1024
	s_add_u32 m0, s26, 65536
	s_nop 0
	global_load_lds_dwordx4 v4, s[22:23]
	global_load_lds_dwordx4 v4, s[22:23] offset:1024
	s_add_u32 m0, s26, 81920
	s_nop 0
	global_load_lds_dwordx4 v4, s[24:25]
	global_load_lds_dwordx4 v4, s[24:25] offset:1024
	v_add_u32_e32 v4, 0x4000, v4
	s_waitcnt vmcnt(6)
	s_barrier
	s_add_u32 m0, s26, 98304
	s_nop 0
	global_load_lds_dwordx4 v4, s[20:21]
	global_load_lds_dwordx4 v4, s[20:21] offset:1024
	s_add_u32 m0, s26, 114688
	s_nop 0
	global_load_lds_dwordx4 v4, s[22:23]
	global_load_lds_dwordx4 v4, s[22:23] offset:1024
	s_add_u32 m0, s26, 131072
	s_nop 0
	global_load_lds_dwordx4 v4, s[24:25]
	global_load_lds_dwordx4 v4, s[24:25] offset:1024
	v_add_u32_e32 v4, 0x4000, v4
	s_add_u32 s32, s28, 0
	s_addc_u32 s33, s29, 0
	global_load_dword v128, v5, s[32:33] nt
	global_load_dword v144, v5, s[32:33] offset:128 nt
	s_add_u32 s34, s28, 16384
	s_addc_u32 s35, s29, 0
	global_load_dword v129, v5, s[34:35] nt
	global_load_dword v145, v5, s[34:35] offset:128 nt
	s_add_u32 s32, s28, 32768
	s_addc_u32 s33, s29, 0
	global_load_dword v130, v5, s[32:33] nt
	global_load_dword v146, v5, s[32:33] offset:128 nt
	s_add_u32 s34, s28, 49152
	s_addc_u32 s35, s29, 0
	global_load_dword v131, v5, s[34:35] nt
	global_load_dword v147, v5, s[34:35] offset:128 nt
	s_add_u32 s32, s28, 131072
	s_addc_u32 s33, s29, 0
	global_load_dword v132, v5, s[32:33] nt
	global_load_dword v148, v5, s[32:33] offset:128 nt
	s_add_u32 s34, s28, 147456
	s_addc_u32 s35, s29, 0
	global_load_dword v133, v5, s[34:35] nt
	global_load_dword v149, v5, s[34:35] offset:128 nt
	s_add_u32 s32, s28, 163840
	s_addc_u32 s33, s29, 0
	global_load_dword v134, v5, s[32:33] nt
	global_load_dword v150, v5, s[32:33] offset:128 nt
	s_add_u32 s34, s28, 180224
	s_addc_u32 s35, s29, 0
	global_load_dword v135, v5, s[34:35] nt
	global_load_dword v151, v5, s[34:35] offset:128 nt
	s_add_u32 s32, s28, 262144
	s_addc_u32 s33, s29, 0
	global_load_dword v136, v5, s[32:33] nt
	global_load_dword v152, v5, s[32:33] offset:128 nt
	s_add_u32 s34, s28, 278528
	s_addc_u32 s35, s29, 0
	global_load_dword v137, v5, s[34:35] nt
	global_load_dword v153, v5, s[34:35] offset:128 nt
	s_add_u32 s32, s28, 294912
	s_addc_u32 s33, s29, 0
	global_load_dword v138, v5, s[32:33] nt
	global_load_dword v154, v5, s[32:33] offset:128 nt
	s_add_u32 s34, s28, 311296
	s_addc_u32 s35, s29, 0
	global_load_dword v139, v5, s[34:35] nt
	global_load_dword v155, v5, s[34:35] offset:128 nt
	s_add_u32 s32, s28, 393216
	s_addc_u32 s33, s29, 0
	global_load_dword v140, v5, s[32:33] nt
	global_load_dword v156, v5, s[32:33] offset:128 nt
	s_add_u32 s34, s28, 409600
	s_addc_u32 s35, s29, 0
	global_load_dword v141, v5, s[34:35] nt
	global_load_dword v157, v5, s[34:35] offset:128 nt
	s_add_u32 s32, s28, 425984
	s_addc_u32 s33, s29, 0
	global_load_dword v142, v5, s[32:33] nt
	global_load_dword v158, v5, s[32:33] offset:128 nt
	s_add_u32 s34, s28, 442368
	s_addc_u32 s35, s29, 0
	global_load_dword v143, v5, s[34:35] nt
	global_load_dword v159, v5, s[34:35] offset:128 nt
	ds_read_b128 v[24:27], v8
	ds_read_b128 v[32:35], v12
	ds_read_b128 v[28:31], v8 offset:4096
	ds_read_b128 v[36:39], v12 offset:4096
	ds_read_b128 v[40:43], v9
	ds_read_b128 v[48:51], v13
	ds_read_b128 v[44:47], v9 offset:4096
	ds_read_b128 v[52:55], v13 offset:4096
	s_waitcnt lgkmcnt(4)
	v_mfma_f32_32x32x16_bf16 v[64:79], v[24:27], v[32:35], 0
	v_mfma_f32_32x32x16_bf16 v[80:95], v[24:27], v[36:39], 0
	v_mfma_f32_32x32x16_bf16 v[96:111], v[28:31], v[32:35], 0
	v_mfma_f32_32x32x16_bf16 v[112:127], v[28:31], v[36:39], 0
	ds_read_b128 v[24:27], v10
	ds_read_b128 v[32:35], v14
	ds_read_b128 v[28:31], v10 offset:4096
	ds_read_b128 v[36:39], v14 offset:4096
	s_waitcnt lgkmcnt(4)
	v_mfma_f32_32x32x16_bf16 v[64:79], v[40:43], v[48:51], v[64:79]
	v_mfma_f32_32x32x16_bf16 v[80:95], v[40:43], v[52:55], v[80:95]
	v_mfma_f32_32x32x16_bf16 v[96:111], v[44:47], v[48:51], v[96:111]
	v_mfma_f32_32x32x16_bf16 v[112:127], v[44:47], v[52:55], v[112:127]
	ds_read_b128 v[40:43], v11
	ds_read_b128 v[48:51], v15
	ds_read_b128 v[44:47], v11 offset:4096
	ds_read_b128 v[52:55], v15 offset:4096
	s_waitcnt lgkmcnt(4)
	v_mfma_f32_32x32x16_bf16 v[64:79], v[24:27], v[32:35], v[64:79]
	v_mfma_f32_32x32x16_bf16 v[80:95], v[24:27], v[36:39], v[80:95]
	v_mfma_f32_32x32x16_bf16 v[96:111], v[28:31], v[32:35], v[96:111]
	v_mfma_f32_32x32x16_bf16 v[112:127], v[28:31], v[36:39], v[112:127]
	s_waitcnt lgkmcnt(0)
	v_mfma_f32_32x32x16_bf16 v[64:79], v[40:43], v[48:51], v[64:79]
	v_mfma_f32_32x32x16_bf16 v[80:95], v[40:43], v[52:55], v[80:95]
	v_mfma_f32_32x32x16_bf16 v[96:111], v[44:47], v[48:51], v[96:111]
	v_mfma_f32_32x32x16_bf16 v[112:127], v[44:47], v[52:55], v[112:127]
	s_waitcnt vmcnt(38)
	s_barrier
	s_add_u32 m0, s26, 0
	s_nop 0
	global_load_lds_dwordx4 v4, s[20:21]
	global_load_lds_dwordx4 v4, s[20:21] offset:1024
	s_add_u32 m0, s26, 16384
	s_nop 0
	global_load_lds_dwordx4 v4, s[22:23]
	global_load_lds_dwordx4 v4, s[22:23] offset:1024
	s_add_u32 m0, s26, 32768
	s_nop 0
	global_load_lds_dwordx4 v4, s[24:25]
	global_load_lds_dwordx4 v4, s[24:25] offset:1024
	v_add_u32_e32 v4, 0x4000, v4
	ds_read_b128 v[24:27], v8 offset:49152
	ds_read_b128 v[32:35], v12 offset:49152
	ds_read_b128 v[28:31], v8 offset:53248
	ds_read_b128 v[36:39], v12 offset:53248
	ds_read_b128 v[40:43], v9 offset:49152
	ds_read_b128 v[48:51], v13 offset:49152
	ds_read_b128 v[44:47], v9 offset:53248
	ds_read_b128 v[52:55], v13 offset:53248
	s_waitcnt lgkmcnt(4)
	v_mfma_f32_32x32x16_bf16 v[64:79], v[24:27], v[32:35], v[64:79]
	v_mfma_f32_32x32x16_bf16 v[80:95], v[24:27], v[36:39], v[80:95]
	v_mfma_f32_32x32x16_bf16 v[96:111], v[28:31], v[32:35], v[96:111]
	v_mfma_f32_32x32x16_bf16 v[112:127], v[28:31], v[36:39], v[112:127]
	ds_read_b128 v[24:27], v10 offset:49152
	ds_read_b128 v[32:35], v14 offset:49152
	ds_read_b128 v[28:31], v10 offset:53248
	ds_read_b128 v[36:39], v14 offset:53248
	s_waitcnt lgkmcnt(4)
	v_mfma_f32_32x32x16_bf16 v[64:79], v[40:43], v[48:51], v[64:79]
	v_mfma_f32_32x32x16_bf16 v[80:95], v[40:43], v[52:55], v[80:95]
	v_mfma_f32_32x32x16_bf16 v[96:111], v[44:47], v[48:51], v[96:111]
	v_mfma_f32_32x32x16_bf16 v[112:127], v[44:47], v[52:55], v[112:127]
	ds_read_b128 v[40:43], v11 offset:49152
	ds_read_b128 v[48:51], v15 offset:49152
	ds_read_b128 v[44:47], v11 offset:53248
	ds_read_b128 v[52:55], v15 offset:53248
	s_waitcnt lgkmcnt(4)
	v_mfma_f32_32x32x16_bf16 v[64:79], v[24:27], v[32:35], v[64:79]
	v_mfma_f32_32x32x16_bf16 v[80:95], v[24:27], v[36:39], v[80:95]
	v_mfma_f32_32x32x16_bf16 v[96:111], v[28:31], v[32:35], v[96:111]
	v_mfma_f32_32x32x16_bf16 v[112:127], v[28:31], v[36:39], v[112:127]
	s_waitcnt lgkmcnt(0)
	v_mfma_f32_32x32x16_bf16 v[64:79], v[40:43], v[48:51], v[64:79]
	v_mfma_f32_32x32x16_bf16 v[80:95], v[40:43], v[52:55], v[80:95]
	v_mfma_f32_32x32x16_bf16 v[96:111], v[44:47], v[48:51], v[96:111]
	v_mfma_f32_32x32x16_bf16 v[112:127], v[44:47], v[52:55], v[112:127]
	s_waitcnt vmcnt(38)
	s_barrier
	s_add_u32 m0, s26, 49152
	s_nop 0
	global_load_lds_dwordx4 v4, s[20:21]
	global_load_lds_dwordx4 v4, s[20:21] offset:1024
	s_add_u32 m0, s26, 65536
	s_nop 0
	global_load_lds_dwordx4 v4, s[22:23]
	global_load_lds_dwordx4 v4, s[22:23] offset:1024
	s_add_u32 m0, s26, 81920
	s_nop 0
	global_load_lds_dwordx4 v4, s[24:25]
	global_load_lds_dwordx4 v4, s[24:25] offset:1024
	v_add_u32_e32 v4, 0x4000, v4
	ds_read_b128 v[24:27], v16 offset:32768
	ds_read_b128 v[32:35], v20 offset:32768
	ds_read_b128 v[28:31], v16 offset:36864
	ds_read_b128 v[36:39], v20 offset:36864
	ds_read_b128 v[40:43], v17 offset:32768
	ds_read_b128 v[48:51], v21 offset:32768
	ds_read_b128 v[44:47], v17 offset:36864
	ds_read_b128 v[52:55], v21 offset:36864
	s_waitcnt lgkmcnt(4)
	v_mfma_f32_32x32x16_bf16 v[64:79], v[24:27], v[32:35], v[64:79]
	v_mfma_f32_32x32x16_bf16 v[80:95], v[24:27], v[36:39], v[80:95]
	v_mfma_f32_32x32x16_bf16 v[96:111], v[28:31], v[32:35], v[96:111]
	v_mfma_f32_32x32x16_bf16 v[112:127], v[28:31], v[36:39], v[112:127]
	ds_read_b128 v[24:27], v18 offset:32768
	ds_read_b128 v[32:35], v22 offset:32768
	ds_read_b128 v[28:31], v18 offset:36864
	ds_read_b128 v[36:39], v22 offset:36864
	s_waitcnt lgkmcnt(4)
	v_mfma_f32_32x32x16_bf16 v[64:79], v[40:43], v[48:51], v[64:79]
	v_mfma_f32_32x32x16_bf16 v[80:95], v[40:43], v[52:55], v[80:95]
	v_mfma_f32_32x32x16_bf16 v[96:111], v[44:47], v[48:51], v[96:111]
	v_mfma_f32_32x32x16_bf16 v[112:127], v[44:47], v[52:55], v[112:127]
	ds_read_b128 v[40:43], v19 offset:32768
	ds_read_b128 v[48:51], v23 offset:32768
	ds_read_b128 v[44:47], v19 offset:36864
	ds_read_b128 v[52:55], v23 offset:36864
	s_waitcnt lgkmcnt(4)
	v_mfma_f32_32x32x16_bf16 v[64:79], v[24:27], v[32:35], v[64:79]
	v_mfma_f32_32x32x16_bf16 v[80:95], v[24:27], v[36:39], v[80:95]
	v_mfma_f32_32x32x16_bf16 v[96:111], v[28:31], v[32:35], v[96:111]
	v_mfma_f32_32x32x16_bf16 v[112:127], v[28:31], v[36:39], v[112:127]
	s_waitcnt lgkmcnt(0)
	v_mfma_f32_32x32x16_bf16 v[64:79], v[40:43], v[48:51], v[64:79]
	v_mfma_f32_32x32x16_bf16 v[80:95], v[40:43], v[52:55], v[80:95]
	v_mfma_f32_32x32x16_bf16 v[96:111], v[44:47], v[48:51], v[96:111]
	v_mfma_f32_32x32x16_bf16 v[112:127], v[44:47], v[52:55], v[112:127]
	s_waitcnt vmcnt(6)
	s_barrier
	s_add_u32 m0, s26, 98304
	s_nop 0
	global_load_lds_dwordx4 v4, s[20:21]
	global_load_lds_dwordx4 v4, s[20:21] offset:1024
	s_add_u32 m0, s26, 114688
	s_nop 0
	global_load_lds_dwordx4 v4, s[22:23]
	global_load_lds_dwordx4 v4, s[22:23] offset:1024
	s_add_u32 m0, s26, 131072
	s_nop 0
	global_load_lds_dwordx4 v4, s[24:25]
	global_load_lds_dwordx4 v4, s[24:25] offset:1024
	v_add_u32_e32 v4, 0x4000, v4
	s_add_u32 s32, s28, 524288
	s_addc_u32 s33, s29, 0
	global_load_dword v160, v5, s[32:33] nt
	global_load_dword v176, v5, s[32:33] offset:128 nt
	s_add_u32 s34, s28, 540672
	s_addc_u32 s35, s29, 0
	global_load_dword v161, v5, s[34:35] nt
	global_load_dword v177, v5, s[34:35] offset:128 nt
	s_add_u32 s32, s28, 557056
	s_addc_u32 s33, s29, 0
	global_load_dword v162, v5, s[32:33] nt
	global_load_dword v178, v5, s[32:33] offset:128 nt
	s_add_u32 s34, s28, 573440
	s_addc_u32 s35, s29, 0
	global_load_dword v163, v5, s[34:35] nt
	global_load_dword v179, v5, s[34:35] offset:128 nt
	s_add_u32 s32, s28, 655360
	s_addc_u32 s33, s29, 0
	global_load_dword v164, v5, s[32:33] nt
	global_load_dword v180, v5, s[32:33] offset:128 nt
	s_add_u32 s34, s28, 671744
	s_addc_u32 s35, s29, 0
	global_load_dword v165, v5, s[34:35] nt
	global_load_dword v181, v5, s[34:35] offset:128 nt
	s_add_u32 s32, s28, 688128
	s_addc_u32 s33, s29, 0
	global_load_dword v166, v5, s[32:33] nt
	global_load_dword v182, v5, s[32:33] offset:128 nt
	s_add_u32 s34, s28, 704512
	s_addc_u32 s35, s29, 0
	global_load_dword v167, v5, s[34:35] nt
	global_load_dword v183, v5, s[34:35] offset:128 nt
	s_add_u32 s32, s28, 786432
	s_addc_u32 s33, s29, 0
	global_load_dword v168, v5, s[32:33] nt
	global_load_dword v184, v5, s[32:33] offset:128 nt
	s_add_u32 s34, s28, 802816
	s_addc_u32 s35, s29, 0
	global_load_dword v169, v5, s[34:35] nt
	global_load_dword v185, v5, s[34:35] offset:128 nt
	s_add_u32 s32, s28, 819200
	s_addc_u32 s33, s29, 0
	global_load_dword v170, v5, s[32:33] nt
	global_load_dword v186, v5, s[32:33] offset:128 nt
	s_add_u32 s34, s28, 835584
	s_addc_u32 s35, s29, 0
	global_load_dword v171, v5, s[34:35] nt
	global_load_dword v187, v5, s[34:35] offset:128 nt
	s_add_u32 s32, s28, 917504
	s_addc_u32 s33, s29, 0
	global_load_dword v172, v5, s[32:33] nt
	global_load_dword v188, v5, s[32:33] offset:128 nt
	s_add_u32 s34, s28, 933888
	s_addc_u32 s35, s29, 0
	global_load_dword v173, v5, s[34:35] nt
	global_load_dword v189, v5, s[34:35] offset:128 nt
	s_add_u32 s32, s28, 950272
	s_addc_u32 s33, s29, 0
	global_load_dword v174, v5, s[32:33] nt
	global_load_dword v190, v5, s[32:33] offset:128 nt
	s_add_u32 s34, s28, 966656
	s_addc_u32 s35, s29, 0
	global_load_dword v175, v5, s[34:35] nt
	global_load_dword v191, v5, s[34:35] offset:128 nt
	ds_read_b128 v[24:27], v8
	ds_read_b128 v[32:35], v12
	ds_read_b128 v[28:31], v8 offset:4096
	ds_read_b128 v[36:39], v12 offset:4096
	ds_read_b128 v[40:43], v9
	ds_read_b128 v[48:51], v13
	ds_read_b128 v[44:47], v9 offset:4096
	ds_read_b128 v[52:55], v13 offset:4096
	s_waitcnt lgkmcnt(4)
	v_mfma_f32_32x32x16_bf16 v[64:79], v[24:27], v[32:35], v[64:79]
	v_mfma_f32_32x32x16_bf16 v[80:95], v[24:27], v[36:39], v[80:95]
	v_mfma_f32_32x32x16_bf16 v[96:111], v[28:31], v[32:35], v[96:111]
	v_mfma_f32_32x32x16_bf16 v[112:127], v[28:31], v[36:39], v[112:127]
	ds_read_b128 v[24:27], v10
	ds_read_b128 v[32:35], v14
	ds_read_b128 v[28:31], v10 offset:4096
	ds_read_b128 v[36:39], v14 offset:4096
	s_waitcnt lgkmcnt(4)
	v_mfma_f32_32x32x16_bf16 v[64:79], v[40:43], v[48:51], v[64:79]
	v_mfma_f32_32x32x16_bf16 v[80:95], v[40:43], v[52:55], v[80:95]
	v_mfma_f32_32x32x16_bf16 v[96:111], v[44:47], v[48:51], v[96:111]
	v_mfma_f32_32x32x16_bf16 v[112:127], v[44:47], v[52:55], v[112:127]
	ds_read_b128 v[40:43], v11
	ds_read_b128 v[48:51], v15
	ds_read_b128 v[44:47], v11 offset:4096
	ds_read_b128 v[52:55], v15 offset:4096
	s_waitcnt lgkmcnt(4)
	v_mfma_f32_32x32x16_bf16 v[64:79], v[24:27], v[32:35], v[64:79]
	v_mfma_f32_32x32x16_bf16 v[80:95], v[24:27], v[36:39], v[80:95]
	v_mfma_f32_32x32x16_bf16 v[96:111], v[28:31], v[32:35], v[96:111]
	v_mfma_f32_32x32x16_bf16 v[112:127], v[28:31], v[36:39], v[112:127]
	s_waitcnt lgkmcnt(0)
	v_mfma_f32_32x32x16_bf16 v[64:79], v[40:43], v[48:51], v[64:79]
	v_mfma_f32_32x32x16_bf16 v[80:95], v[40:43], v[52:55], v[80:95]
	v_mfma_f32_32x32x16_bf16 v[96:111], v[44:47], v[48:51], v[96:111]
	v_mfma_f32_32x32x16_bf16 v[112:127], v[44:47], v[52:55], v[112:127]
	s_waitcnt vmcnt(38)
	s_barrier
	s_add_u32 m0, s26, 0
	s_nop 0
	global_load_lds_dwordx4 v4, s[20:21]
	global_load_lds_dwordx4 v4, s[20:21] offset:1024
	s_add_u32 m0, s26, 16384
	s_nop 0
	global_load_lds_dwordx4 v4, s[22:23]
	global_load_lds_dwordx4 v4, s[22:23] offset:1024
	s_add_u32 m0, s26, 32768
	s_nop 0
	global_load_lds_dwordx4 v4, s[24:25]
	global_load_lds_dwordx4 v4, s[24:25] offset:1024
	v_add_u32_e32 v4, 0x4000, v4
	ds_read_b128 v[24:27], v8 offset:49152
	ds_read_b128 v[32:35], v12 offset:49152
	ds_read_b128 v[28:31], v8 offset:53248
	ds_read_b128 v[36:39], v12 offset:53248
	ds_read_b128 v[40:43], v9 offset:49152
	ds_read_b128 v[48:51], v13 offset:49152
	ds_read_b128 v[44:47], v9 offset:53248
	ds_read_b128 v[52:55], v13 offset:53248
	s_waitcnt lgkmcnt(4)
	v_mfma_f32_32x32x16_bf16 v[64:79], v[24:27], v[32:35], v[64:79]
	v_mfma_f32_32x32x16_bf16 v[80:95], v[24:27], v[36:39], v[80:95]
	v_mfma_f32_32x32x16_bf16 v[96:111], v[28:31], v[32:35], v[96:111]
	v_mfma_f32_32x32x16_bf16 v[112:127], v[28:31], v[36:39], v[112:127]
	ds_read_b128 v[24:27], v10 offset:49152
	ds_read_b128 v[32:35], v14 offset:49152
	ds_read_b128 v[28:31], v10 offset:53248
	ds_read_b128 v[36:39], v14 offset:53248
	s_waitcnt lgkmcnt(4)
	v_mfma_f32_32x32x16_bf16 v[64:79], v[40:43], v[48:51], v[64:79]
	v_mfma_f32_32x32x16_bf16 v[80:95], v[40:43], v[52:55], v[80:95]
	v_mfma_f32_32x32x16_bf16 v[96:111], v[44:47], v[48:51], v[96:111]
	v_mfma_f32_32x32x16_bf16 v[112:127], v[44:47], v[52:55], v[112:127]
	ds_read_b128 v[40:43], v11 offset:49152
	ds_read_b128 v[48:51], v15 offset:49152
	ds_read_b128 v[44:47], v11 offset:53248
	ds_read_b128 v[52:55], v15 offset:53248
	s_waitcnt lgkmcnt(4)
	v_mfma_f32_32x32x16_bf16 v[64:79], v[24:27], v[32:35], v[64:79]
	v_mfma_f32_32x32x16_bf16 v[80:95], v[24:27], v[36:39], v[80:95]
	v_mfma_f32_32x32x16_bf16 v[96:111], v[28:31], v[32:35], v[96:111]
	v_mfma_f32_32x32x16_bf16 v[112:127], v[28:31], v[36:39], v[112:127]
	s_waitcnt lgkmcnt(0)
	v_mfma_f32_32x32x16_bf16 v[64:79], v[40:43], v[48:51], v[64:79]
	v_mfma_f32_32x32x16_bf16 v[80:95], v[40:43], v[52:55], v[80:95]
	v_mfma_f32_32x32x16_bf16 v[96:111], v[44:47], v[48:51], v[96:111]
	v_mfma_f32_32x32x16_bf16 v[112:127], v[44:47], v[52:55], v[112:127]
	s_waitcnt vmcnt(38)
	s_barrier
	s_add_u32 m0, s26, 49152
	s_nop 0
	global_load_lds_dwordx4 v4, s[20:21]
	global_load_lds_dwordx4 v4, s[20:21] offset:1024
	s_add_u32 m0, s26, 65536
	s_nop 0
	global_load_lds_dwordx4 v4, s[22:23]
	global_load_lds_dwordx4 v4, s[22:23] offset:1024
	s_add_u32 m0, s26, 81920
	s_nop 0
	global_load_lds_dwordx4 v4, s[24:25]
	global_load_lds_dwordx4 v4, s[24:25] offset:1024
	v_add_u32_e32 v4, 0x4000, v4
	ds_read_b128 v[24:27], v16 offset:32768
	ds_read_b128 v[32:35], v20 offset:32768
	ds_read_b128 v[28:31], v16 offset:36864
	ds_read_b128 v[36:39], v20 offset:36864
	ds_read_b128 v[40:43], v17 offset:32768
	ds_read_b128 v[48:51], v21 offset:32768
	ds_read_b128 v[44:47], v17 offset:36864
	ds_read_b128 v[52:55], v21 offset:36864
	s_waitcnt lgkmcnt(4)
	v_mfma_f32_32x32x16_bf16 v[64:79], v[24:27], v[32:35], v[64:79]
	v_mfma_f32_32x32x16_bf16 v[80:95], v[24:27], v[36:39], v[80:95]
	v_mfma_f32_32x32x16_bf16 v[96:111], v[28:31], v[32:35], v[96:111]
	v_mfma_f32_32x32x16_bf16 v[112:127], v[28:31], v[36:39], v[112:127]
	ds_read_b128 v[24:27], v18 offset:32768
	ds_read_b128 v[32:35], v22 offset:32768
	ds_read_b128 v[28:31], v18 offset:36864
	ds_read_b128 v[36:39], v22 offset:36864
	s_waitcnt lgkmcnt(4)
	v_mfma_f32_32x32x16_bf16 v[64:79], v[40:43], v[48:51], v[64:79]
	v_mfma_f32_32x32x16_bf16 v[80:95], v[40:43], v[52:55], v[80:95]
	v_mfma_f32_32x32x16_bf16 v[96:111], v[44:47], v[48:51], v[96:111]
	v_mfma_f32_32x32x16_bf16 v[112:127], v[44:47], v[52:55], v[112:127]
	ds_read_b128 v[40:43], v19 offset:32768
	ds_read_b128 v[48:51], v23 offset:32768
	ds_read_b128 v[44:47], v19 offset:36864
	ds_read_b128 v[52:55], v23 offset:36864
	s_waitcnt lgkmcnt(4)
	v_mfma_f32_32x32x16_bf16 v[64:79], v[24:27], v[32:35], v[64:79]
	v_mfma_f32_32x32x16_bf16 v[80:95], v[24:27], v[36:39], v[80:95]
	v_mfma_f32_32x32x16_bf16 v[96:111], v[28:31], v[32:35], v[96:111]
	v_mfma_f32_32x32x16_bf16 v[112:127], v[28:31], v[36:39], v[112:127]
	s_waitcnt lgkmcnt(0)
	v_mfma_f32_32x32x16_bf16 v[64:79], v[40:43], v[48:51], v[64:79]
	v_mfma_f32_32x32x16_bf16 v[80:95], v[40:43], v[52:55], v[80:95]
	v_mfma_f32_32x32x16_bf16 v[96:111], v[44:47], v[48:51], v[96:111]
	v_mfma_f32_32x32x16_bf16 v[112:127], v[44:47], v[52:55], v[112:127]
	s_waitcnt vmcnt(6)
	s_barrier
	ds_read_b128 v[24:27], v8
	ds_read_b128 v[32:35], v12
	ds_read_b128 v[28:31], v8 offset:4096
	ds_read_b128 v[36:39], v12 offset:4096
	ds_read_b128 v[40:43], v9
	ds_read_b128 v[48:51], v13
	ds_read_b128 v[44:47], v9 offset:4096
	ds_read_b128 v[52:55], v13 offset:4096
	s_waitcnt lgkmcnt(4)
	v_mfma_f32_32x32x16_bf16 v[64:79], v[24:27], v[32:35], v[64:79]
	v_mfma_f32_32x32x16_bf16 v[80:95], v[24:27], v[36:39], v[80:95]
	v_mfma_f32_32x32x16_bf16 v[96:111], v[28:31], v[32:35], v[96:111]
	v_mfma_f32_32x32x16_bf16 v[112:127], v[28:31], v[36:39], v[112:127]
	ds_read_b128 v[24:27], v10
	ds_read_b128 v[32:35], v14
	ds_read_b128 v[28:31], v10 offset:4096
	ds_read_b128 v[36:39], v14 offset:4096
	s_waitcnt lgkmcnt(4)
	v_mfma_f32_32x32x16_bf16 v[64:79], v[40:43], v[48:51], v[64:79]
	v_mfma_f32_32x32x16_bf16 v[80:95], v[40:43], v[52:55], v[80:95]
	v_mfma_f32_32x32x16_bf16 v[96:111], v[44:47], v[48:51], v[96:111]
	v_mfma_f32_32x32x16_bf16 v[112:127], v[44:47], v[52:55], v[112:127]
	ds_read_b128 v[40:43], v11
	ds_read_b128 v[48:51], v15
	ds_read_b128 v[44:47], v11 offset:4096
	ds_read_b128 v[52:55], v15 offset:4096
	s_waitcnt lgkmcnt(4)
	v_mfma_f32_32x32x16_bf16 v[64:79], v[24:27], v[32:35], v[64:79]
	v_mfma_f32_32x32x16_bf16 v[80:95], v[24:27], v[36:39], v[80:95]
	v_mfma_f32_32x32x16_bf16 v[96:111], v[28:31], v[32:35], v[96:111]
	v_mfma_f32_32x32x16_bf16 v[112:127], v[28:31], v[36:39], v[112:127]
	s_waitcnt lgkmcnt(0)
	v_mfma_f32_32x32x16_bf16 v[64:79], v[40:43], v[48:51], v[64:79]
	v_mfma_f32_32x32x16_bf16 v[80:95], v[40:43], v[52:55], v[80:95]
	v_mfma_f32_32x32x16_bf16 v[96:111], v[44:47], v[48:51], v[96:111]
	v_mfma_f32_32x32x16_bf16 v[112:127], v[44:47], v[52:55], v[112:127]
	s_waitcnt vmcnt(0)
	s_barrier
	ds_read_b128 v[24:27], v8 offset:49152
	ds_read_b128 v[32:35], v12 offset:49152
	ds_read_b128 v[28:31], v8 offset:53248
	ds_read_b128 v[36:39], v12 offset:53248
	ds_read_b128 v[40:43], v9 offset:49152
	ds_read_b128 v[48:51], v13 offset:49152
	ds_read_b128 v[44:47], v9 offset:53248
	ds_read_b128 v[52:55], v13 offset:53248
	s_waitcnt lgkmcnt(4)
	v_mfma_f32_32x32x16_bf16 v[64:79], v[24:27], v[32:35], v[64:79]
	v_mfma_f32_32x32x16_bf16 v[80:95], v[24:27], v[36:39], v[80:95]
	v_mfma_f32_32x32x16_bf16 v[96:111], v[28:31], v[32:35], v[96:111]
	v_mfma_f32_32x32x16_bf16 v[112:127], v[28:31], v[36:39], v[112:127]
	ds_read_b128 v[24:27], v10 offset:49152
	ds_read_b128 v[32:35], v14 offset:49152
	ds_read_b128 v[28:31], v10 offset:53248
	ds_read_b128 v[36:39], v14 offset:53248
	s_waitcnt lgkmcnt(4)
	v_mfma_f32_32x32x16_bf16 v[64:79], v[40:43], v[48:51], v[64:79]
	v_mfma_f32_32x32x16_bf16 v[80:95], v[40:43], v[52:55], v[80:95]
	v_mfma_f32_32x32x16_bf16 v[96:111], v[44:47], v[48:51], v[96:111]
	v_mfma_f32_32x32x16_bf16 v[112:127], v[44:47], v[52:55], v[112:127]
	ds_read_b128 v[40:43], v11 offset:49152
	ds_read_b128 v[48:51], v15 offset:49152
	ds_read_b128 v[44:47], v11 offset:53248
	ds_read_b128 v[52:55], v15 offset:53248
	s_waitcnt lgkmcnt(4)
	v_mfma_f32_32x32x16_bf16 v[64:79], v[24:27], v[32:35], v[64:79]
	v_mfma_f32_32x32x16_bf16 v[80:95], v[24:27], v[36:39], v[80:95]
	v_mfma_f32_32x32x16_bf16 v[96:111], v[28:31], v[32:35], v[96:111]
	v_mfma_f32_32x32x16_bf16 v[112:127], v[28:31], v[36:39], v[112:127]
	s_waitcnt lgkmcnt(0)
	v_mfma_f32_32x32x16_bf16 v[64:79], v[40:43], v[48:51], v[64:79]
	v_mfma_f32_32x32x16_bf16 v[80:95], v[40:43], v[52:55], v[80:95]
	v_mfma_f32_32x32x16_bf16 v[96:111], v[44:47], v[48:51], v[96:111]
	v_mfma_f32_32x32x16_bf16 v[112:127], v[44:47], v[52:55], v[112:127]
	s_nop 15
	s_nop 3
	s_add_u32 s32, s30, 0
	s_addc_u32 s33, s31, 0
	v_add_f32_e32 v64, v64, v62
	v_add_f32_e32 v64, v64, v128
	v_add_f32_e32 v80, v80, v63
	v_add_f32_e32 v80, v80, v144
	global_store_dword v5, v64, s[32:33] sc1
	global_store_dword v5, v80, s[32:33] offset:128 sc1
	s_add_u32 s34, s30, 16384
	s_addc_u32 s35, s31, 0
	v_add_f32_e32 v65, v65, v62
	v_add_f32_e32 v65, v65, v129
	v_add_f32_e32 v81, v81, v63
	v_add_f32_e32 v81, v81, v145
	global_store_dword v5, v65, s[34:35] sc1
	global_store_dword v5, v81, s[34:35] offset:128 sc1
	s_add_u32 s32, s30, 32768
	s_addc_u32 s33, s31, 0
	v_add_f32_e32 v66, v66, v62
	v_add_f32_e32 v66, v66, v130
	v_add_f32_e32 v82, v82, v63
	v_add_f32_e32 v82, v82, v146
	global_store_dword v5, v66, s[32:33] sc1
	global_store_dword v5, v82, s[32:33] offset:128 sc1
	s_add_u32 s34, s30, 49152
	s_addc_u32 s35, s31, 0
	v_add_f32_e32 v67, v67, v62
	v_add_f32_e32 v67, v67, v131
	v_add_f32_e32 v83, v83, v63
	v_add_f32_e32 v83, v83, v147
	global_store_dword v5, v67, s[34:35] sc1
	global_store_dword v5, v83, s[34:35] offset:128 sc1
	s_add_u32 s32, s30, 131072
	s_addc_u32 s33, s31, 0
	v_add_f32_e32 v68, v68, v62
	v_add_f32_e32 v68, v68, v132
	v_add_f32_e32 v84, v84, v63
	v_add_f32_e32 v84, v84, v148
	global_store_dword v5, v68, s[32:33] sc1
	global_store_dword v5, v84, s[32:33] offset:128 sc1
	s_add_u32 s34, s30, 147456
	s_addc_u32 s35, s31, 0
	v_add_f32_e32 v69, v69, v62
	v_add_f32_e32 v69, v69, v133
	v_add_f32_e32 v85, v85, v63
	v_add_f32_e32 v85, v85, v149
	global_store_dword v5, v69, s[34:35] sc1
	global_store_dword v5, v85, s[34:35] offset:128 sc1
	s_add_u32 s32, s30, 163840
	s_addc_u32 s33, s31, 0
	v_add_f32_e32 v70, v70, v62
	v_add_f32_e32 v70, v70, v134
	v_add_f32_e32 v86, v86, v63
	v_add_f32_e32 v86, v86, v150
	global_store_dword v5, v70, s[32:33] sc1
	global_store_dword v5, v86, s[32:33] offset:128 sc1
	s_add_u32 s34, s30, 180224
	s_addc_u32 s35, s31, 0
	v_add_f32_e32 v71, v71, v62
	v_add_f32_e32 v71, v71, v135
	v_add_f32_e32 v87, v87, v63
	v_add_f32_e32 v87, v87, v151
	global_store_dword v5, v71, s[34:35] sc1
	global_store_dword v5, v87, s[34:35] offset:128 sc1
	s_add_u32 s32, s30, 262144
	s_addc_u32 s33, s31, 0
	v_add_f32_e32 v72, v72, v62
	v_add_f32_e32 v72, v72, v136
	v_add_f32_e32 v88, v88, v63
	v_add_f32_e32 v88, v88, v152
	global_store_dword v5, v72, s[32:33] sc1
	global_store_dword v5, v88, s[32:33] offset:128 sc1
	s_add_u32 s34, s30, 278528
	s_addc_u32 s35, s31, 0
	v_add_f32_e32 v73, v73, v62
	v_add_f32_e32 v73, v73, v137
	v_add_f32_e32 v89, v89, v63
	v_add_f32_e32 v89, v89, v153
	global_store_dword v5, v73, s[34:35] sc1
	global_store_dword v5, v89, s[34:35] offset:128 sc1
	s_add_u32 s32, s30, 294912
	s_addc_u32 s33, s31, 0
	v_add_f32_e32 v74, v74, v62
	v_add_f32_e32 v74, v74, v138
	v_add_f32_e32 v90, v90, v63
	v_add_f32_e32 v90, v90, v154
	global_store_dword v5, v74, s[32:33] sc1
	global_store_dword v5, v90, s[32:33] offset:128 sc1
	s_add_u32 s34, s30, 311296
	s_addc_u32 s35, s31, 0
	v_add_f32_e32 v75, v75, v62
	v_add_f32_e32 v75, v75, v139
	v_add_f32_e32 v91, v91, v63
	v_add_f32_e32 v91, v91, v155
	global_store_dword v5, v75, s[34:35] sc1
	global_store_dword v5, v91, s[34:35] offset:128 sc1
	s_add_u32 s32, s30, 393216
	s_addc_u32 s33, s31, 0
	v_add_f32_e32 v76, v76, v62
	v_add_f32_e32 v76, v76, v140
	v_add_f32_e32 v92, v92, v63
	v_add_f32_e32 v92, v92, v156
	global_store_dword v5, v76, s[32:33] sc1
	global_store_dword v5, v92, s[32:33] offset:128 sc1
	s_add_u32 s34, s30, 409600
	s_addc_u32 s35, s31, 0
	v_add_f32_e32 v77, v77, v62
	v_add_f32_e32 v77, v77, v141
	v_add_f32_e32 v93, v93, v63
	v_add_f32_e32 v93, v93, v157
	global_store_dword v5, v77, s[34:35] sc1
	global_store_dword v5, v93, s[34:35] offset:128 sc1
	s_add_u32 s32, s30, 425984
	s_addc_u32 s33, s31, 0
	v_add_f32_e32 v78, v78, v62
	v_add_f32_e32 v78, v78, v142
	v_add_f32_e32 v94, v94, v63
	v_add_f32_e32 v94, v94, v158
	global_store_dword v5, v78, s[32:33] sc1
	global_store_dword v5, v94, s[32:33] offset:128 sc1
	s_add_u32 s34, s30, 442368
	s_addc_u32 s35, s31, 0
	v_add_f32_e32 v79, v79, v62
	v_add_f32_e32 v79, v79, v143
	v_add_f32_e32 v95, v95, v63
	v_add_f32_e32 v95, v95, v159
	global_store_dword v5, v79, s[34:35] sc1
	global_store_dword v5, v95, s[34:35] offset:128 sc1
	s_add_u32 s32, s30, 524288
	s_addc_u32 s33, s31, 0
	v_add_f32_e32 v96, v96, v62
	v_add_f32_e32 v96, v96, v160
	v_add_f32_e32 v112, v112, v63
	v_add_f32_e32 v112, v112, v176
	global_store_dword v5, v96, s[32:33] sc1
	global_store_dword v5, v112, s[32:33] offset:128 sc1
	s_add_u32 s34, s30, 540672
	s_addc_u32 s35, s31, 0
	v_add_f32_e32 v97, v97, v62
	v_add_f32_e32 v97, v97, v161
	v_add_f32_e32 v113, v113, v63
	v_add_f32_e32 v113, v113, v177
	global_store_dword v5, v97, s[34:35] sc1
	global_store_dword v5, v113, s[34:35] offset:128 sc1
	s_add_u32 s32, s30, 557056
	s_addc_u32 s33, s31, 0
	v_add_f32_e32 v98, v98, v62
	v_add_f32_e32 v98, v98, v162
	v_add_f32_e32 v114, v114, v63
	v_add_f32_e32 v114, v114, v178
	global_store_dword v5, v98, s[32:33] sc1
	global_store_dword v5, v114, s[32:33] offset:128 sc1
	s_add_u32 s34, s30, 573440
	s_addc_u32 s35, s31, 0
	v_add_f32_e32 v99, v99, v62
	v_add_f32_e32 v99, v99, v163
	v_add_f32_e32 v115, v115, v63
	v_add_f32_e32 v115, v115, v179
	global_store_dword v5, v99, s[34:35] sc1
	global_store_dword v5, v115, s[34:35] offset:128 sc1
	s_add_u32 s32, s30, 655360
	s_addc_u32 s33, s31, 0
	v_add_f32_e32 v100, v100, v62
	v_add_f32_e32 v100, v100, v164
	v_add_f32_e32 v116, v116, v63
	v_add_f32_e32 v116, v116, v180
	global_store_dword v5, v100, s[32:33] sc1
	global_store_dword v5, v116, s[32:33] offset:128 sc1
	s_add_u32 s34, s30, 671744
	s_addc_u32 s35, s31, 0
	v_add_f32_e32 v101, v101, v62
	v_add_f32_e32 v101, v101, v165
	v_add_f32_e32 v117, v117, v63
	v_add_f32_e32 v117, v117, v181
	global_store_dword v5, v101, s[34:35] sc1
	global_store_dword v5, v117, s[34:35] offset:128 sc1
	s_add_u32 s32, s30, 688128
	s_addc_u32 s33, s31, 0
	v_add_f32_e32 v102, v102, v62
	v_add_f32_e32 v102, v102, v166
	v_add_f32_e32 v118, v118, v63
	v_add_f32_e32 v118, v118, v182
	global_store_dword v5, v102, s[32:33] sc1
	global_store_dword v5, v118, s[32:33] offset:128 sc1
	s_add_u32 s34, s30, 704512
	s_addc_u32 s35, s31, 0
	v_add_f32_e32 v103, v103, v62
	v_add_f32_e32 v103, v103, v167
	v_add_f32_e32 v119, v119, v63
	v_add_f32_e32 v119, v119, v183
	global_store_dword v5, v103, s[34:35] sc1
	global_store_dword v5, v119, s[34:35] offset:128 sc1
	s_add_u32 s32, s30, 786432
	s_addc_u32 s33, s31, 0
	v_add_f32_e32 v104, v104, v62
	v_add_f32_e32 v104, v104, v168
	v_add_f32_e32 v120, v120, v63
	v_add_f32_e32 v120, v120, v184
	global_store_dword v5, v104, s[32:33] sc1
	global_store_dword v5, v120, s[32:33] offset:128 sc1
	s_add_u32 s34, s30, 802816
	s_addc_u32 s35, s31, 0
	v_add_f32_e32 v105, v105, v62
	v_add_f32_e32 v105, v105, v169
	v_add_f32_e32 v121, v121, v63
	v_add_f32_e32 v121, v121, v185
	global_store_dword v5, v105, s[34:35] sc1
	global_store_dword v5, v121, s[34:35] offset:128 sc1
	s_add_u32 s32, s30, 819200
	s_addc_u32 s33, s31, 0
	v_add_f32_e32 v106, v106, v62
	v_add_f32_e32 v106, v106, v170
	v_add_f32_e32 v122, v122, v63
	v_add_f32_e32 v122, v122, v186
	global_store_dword v5, v106, s[32:33] sc1
	global_store_dword v5, v122, s[32:33] offset:128 sc1
	s_add_u32 s34, s30, 835584
	s_addc_u32 s35, s31, 0
	v_add_f32_e32 v107, v107, v62
	v_add_f32_e32 v107, v107, v171
	v_add_f32_e32 v123, v123, v63
	v_add_f32_e32 v123, v123, v187
	global_store_dword v5, v107, s[34:35] sc1
	global_store_dword v5, v123, s[34:35] offset:128 sc1
	s_add_u32 s32, s30, 917504
	s_addc_u32 s33, s31, 0
	v_add_f32_e32 v108, v108, v62
	v_add_f32_e32 v108, v108, v172
	v_add_f32_e32 v124, v124, v63
	v_add_f32_e32 v124, v124, v188
	global_store_dword v5, v108, s[32:33] sc1
	global_store_dword v5, v124, s[32:33] offset:128 sc1
	s_add_u32 s34, s30, 933888
	s_addc_u32 s35, s31, 0
	v_add_f32_e32 v109, v109, v62
	v_add_f32_e32 v109, v109, v173
	v_add_f32_e32 v125, v125, v63
	v_add_f32_e32 v125, v125, v189
	global_store_dword v5, v109, s[34:35] sc1
	global_store_dword v5, v125, s[34:35] offset:128 sc1
	s_add_u32 s32, s30, 950272
	s_addc_u32 s33, s31, 0
	v_add_f32_e32 v110, v110, v62
	v_add_f32_e32 v110, v110, v174
	v_add_f32_e32 v126, v126, v63
	v_add_f32_e32 v126, v126, v190
	global_store_dword v5, v110, s[32:33] sc1
	global_store_dword v5, v126, s[32:33] offset:128 sc1
	s_add_u32 s34, s30, 966656
	s_addc_u32 s35, s31, 0
	v_add_f32_e32 v111, v111, v62
	v_add_f32_e32 v111, v111, v175
	v_add_f32_e32 v127, v127, v63
	v_add_f32_e32 v127, v127, v191
	global_store_dword v5, v111, s[34:35] sc1
	global_store_dword v5, v127, s[34:35] offset:128 sc1
